# v7 + balanced phase-2 conversion slots (1328/1328/1312 block jobs)
# baseline (speedup 1.0000x reference)
; #define LAS __attribute__((address_space(3)))
; #define PG8_ROWS(x0, uidx) do { ro[x0] = (unsigned)g.rowtab[(uidx) * 256 + Rl + 64 * (x0)]; ro[(x0) + 1] = (unsigned)g.rowtab[(uidx) * 256 + Rl + 64 * (x0) + 64]; } while (0)
; #define PG8_STAGE(bufoff, gbase, voff) do { _Pragma("unroll") for (int _i = 0; _i < 2; ++_i) \
;         __builtin_amdgcn_global_load_lds((const unsigned*)(sbase((const char*)(gbase) + _i * pstep) + (voff)), (LAS unsigned*)(lds + (bufoff) + ldsw + _i * 8192), 16, 0, 0); } while (0)
; #define PG8_WAIT_V(n) asm volatile("s_waitcnt vmcnt(" #n ")" ::: "memory")
; #define PG8_BAR __builtin_amdgcn_s_barrier()
; template <bool FP8, bool GATHER, class Epi, class Sched>
; __device__ __forceinline__ void gemm_phase(LAS unsigned char* lds, const Gemm g, const Sched& S, const Epi& E) {
;     ...
;     const char* cA = (const char*)g.A + (size_t)cur.pm * tstep; const char* cB = (const char*)g.Bt + (size_t)cur.e * estep + (size_t)cur.pn * tstep;
;     const char* nA = cA;
;     if constexpr (GATHER) { PG8_ROWS(0, 0); PG8_ROWS(2, 0); }
;     PG8_STAGE(PG8_SB(0, 0), cB, voffB); PG8_STAGEA(PG8_SA(0, 0), false, 0, 0); PG8_STAGE(PG8_SB(0, 1), cB + hstep, voffB); PG8_STAGEA(PG8_SA(0, 1), false, 1, 0);
;     if (wr == 1) PG8_BAR;
;     PG8_WAIT_V(4); PG8_BAR;
;     PG8_STAGE(PG8_SB(1, 0), cB + kstep, voffB); PG8_STAGEA(PG8_SA(1, 0), false, 0, kstep); PG8_STAGE(PG8_SB(1, 1), cB + hstep + kstep, voffB);
;     PG8_WAIT_V(6); PG8_BAR;
; __device__ __forceinline__ void conv_share_blk(const Args& a, LAS unsigned char* lds, int blk, int G) {
;     const int s = blk % 3, r = blk / 3, nb = (G - s + 2) / 3, nj = CONV_JOBS - BJOB0, j0 = BJOB0 + s * (nj / 3), j1 = (s == 2) ? CONV_JOBS : BJOB0 + (s + 1) * (nj / 3);
;     LAS unsigned char* Tlo = lds + 3 * 16384; LAS unsigned char* Thi = lds + LDS_EXTRA;
;     int j = j0 + r; if (j >= j1) return;
;     f32x4 v[16]; u32x4 o[4]; BJob cc = bjob_addr(a, j);
;     bjob_load(cc, v);
.LBB0_168:
	v_and_b32_e32 v1, 48, v0
	v_lshlrev_b32_e32 v2, 6, v0
	s_movk_i32 s2, 0x3c0
	s_add_u32 s14, s74, 0x3300000
	v_and_or_b32 v1, v2, s2, v1
	v_lshlrev_b32_e32 v2, 2, v0
	s_addc_u32 s15, s75, 0
	s_lshl_b32 s1, s5, 13
	v_and_b32_e32 v2, 32, v2
	v_bitop3_b32 v4, v1, s1, v2 bitop3:0xde
	s_lshl_b32 s1, s3, 5
	s_and_b32 s83, s1, 0x60
	s_lshl_b32 s82, s5, 6
	s_lshl_b32 s1, s83, 7
	s_sext_i32_i16 s6, s4
	s_add_u32 s4, s54, 0x80
	s_addc_u32 s5, s55, 0
	s_waitcnt vmcnt(4)
	s_barrier
	s_add_i32 m0, s78, 0x18000
	v_bitop3_b32 v1, s1, v1, v2 bitop3:0xf6
	v_lshl_add_u64 v[2:3], s[4:5], 0, v[130:131]
	s_add_u32 s4, s54, 0x40080
	s_addc_u32 s5, s55, 0
	global_load_lds_dwordx4 v[2:3], off
	s_add_i32 m0, s78, 0x1a000
	v_lshl_add_u64 v[2:3], s[4:5], 0, v[130:131]
	s_add_u32 s4, s56, 0x80
	s_addc_u32 s5, s57, 0
	global_load_lds_dwordx4 v[2:3], off
	s_add_i32 s84, s78, 0x8000
	v_lshl_add_u64 v[2:3], s[4:5], 0, v[132:133]
	s_add_u32 s4, s56, 0x40080
	s_mov_b32 m0, s84
	s_addc_u32 s5, s57, 0
	global_load_lds_dwordx4 v[2:3], off
	s_add_i32 s85, s78, 0xa000
	v_lshl_add_u64 v[2:3], s[4:5], 0, v[132:133]
	s_add_u32 s4, s54, 0x80080
	s_mov_b32 m0, s85
	s_addc_u32 s5, s55, 0
	global_load_lds_dwordx4 v[2:3], off
	s_add_i32 m0, s78, 0x1c000
	s_mul_hi_u32 s1, s96, 0xaaaaaaab
	v_lshl_add_u64 v[2:3], s[4:5], 0, v[130:131]
	s_add_u32 s4, s54, 0xc0080
	s_addc_u32 s5, s55, 0
	global_load_lds_dwordx4 v[2:3], off
	s_add_i32 m0, s78, 0x1e000
	v_lshl_add_u64 v[2:3], s[4:5], 0, v[130:131]
	global_load_lds_dwordx4 v[2:3], off
	s_lshr_b32 s1, s1, 1
	s_mul_i32 s1, s1, 3
	s_sub_i32 s86, s96, s1
	s_movk_i32 s1, 0x100
	v_cmp_gt_u32_e64 s[2:3], s1, v0
	s_mul_hi_i32 s1, s96, 0x55555556
	v_and_b32_e32 v2, 0x100, v0
	v_writelane_b32 v255, s2, 24
	v_cmp_ne_u32_e64 s[20:21], 0, v2
	s_waitcnt vmcnt(6)
	v_mov_b64_e32 v[136:137], 0x300
	v_writelane_b32 v255, s3, 25
	s_lshr_b32 s2, s1, 31
	s_add_i32 s1, s1, s2
	s_mul_i32 s2, s1, 3
	s_sub_i32 s2, s96, s2
	s_mul_i32 s3, s2, 0x530
	s_add_i32 s87, s3, 0x15b0
	s_min_i32 s87, s87, 0x2000
	s_add_i32 s3, s1, s3
	s_add_i32 s7, s3, 0x1080
	s_cmpk_lt_i32 s7, 0x2000
	s_cselect_b64 s[4:5], -1, 0
	s_waitcnt lgkmcnt(0)
	s_sub_i32 s2, s26, s2
	s_addk_i32 s3, 0xf080
	s_add_i32 s2, s2, 2
	s_lshr_b32 s12, s3, 7
	s_lshl_b32 s3, s7, 8
	s_lshl_b32 s8, s7, 4
	s_ashr_i32 s16, s7, 8
	s_lshl_b32 s7, s7, 3
	s_mul_hi_i32 s89, s2, 0x55555556
	s_and_b32 s22, s8, 0x780
	s_lshl_b64 s[8:9], s[12:13], 24
	s_lshl_b64 s[10:11], s[12:13], 22
	s_lshl_b32 s12, s1, 8
	s_ashr_i32 s17, s16, 31
	s_and_b32 s7, s7, 0x780
	s_lshr_b32 s2, s89, 31
	s_and_b32 s3, s3, 0x700
	s_lshl_b32 s23, s22, 13
	s_and_b32 s12, s12, 0xf00
	s_lshl_b64 s[18:19], s[16:17], 25
	s_lshl_b32 s24, s7, 14
	s_lshl_b64 s[16:17], s[16:17], 23
	v_writelane_b32 v255, s20, 26
	s_ashr_i32 s88, s26, 31
	s_add_i32 s89, s89, s2
	v_writelane_b32 v255, s21, 27
	s_and_b64 s[20:21], s[4:5], exec
	s_cselect_b32 s8, s18, s8
	s_cselect_b32 s90, s12, s3
	s_mov_b32 s3, 0xb300000
	s_cselect_b32 s10, s16, s10
	s_cselect_b32 s16, s46, s50
	s_cselect_b32 s2, s19, s9
	s_cselect_b32 s9, 0, 0
	s_cselect_b32 s18, s24, s23
	s_cselect_b32 s3, s3, 0x2b300000
	s_cselect_b32 s11, s17, s11
	s_cselect_b32 s7, s7, s22
	s_cselect_b32 s12, s47, s51
	s_add_u32 s8, s16, s8
	s_addc_u32 s2, s12, s2
	s_add_u32 s8, s8, s18
	s_addc_u32 s2, s2, s9
	s_lshl_b32 s12, s90, 2
	s_add_u32 s16, s8, s12
	s_addc_u32 s17, s2, 0
	s_add_u32 s2, s74, s3
	s_addc_u32 s3, s75, 0
	s_add_u32 s2, s2, s10
	s_addc_u32 s3, s3, s11
	s_add_u32 s18, s2, s7
	s_addc_u32 s19, s3, s9
	v_cndmask_b32_e64 v144, 0, 1, s[4:5]
	s_and_b64 s[4:5], s[4:5], exec
	s_cselect_b32 s91, 12, 11
	s_add_u32 s92, s74, 0x2b300000
	s_addc_u32 s93, s75, 0
	s_add_u32 s94, s74, 0xb300000
	s_mul_i32 s3, s96, 0x530
	s_mulk_i32 s1, 0xf8f
	s_addc_u32 s95, s75, 0
	s_sub_i32 s2, s3, s1
	s_add_i32 s3, s89, s3
	s_sub_i32 s1, s3, s1
	s_addk_i32 s1, 0x1080
	v_writelane_b32 v255, s2, 28
	s_lshl_b32 s2, s1, 8
	s_add_i32 s29, 0, 0x10000
	s_add_i32 s24, 0, 0x14000
	v_writelane_b32 v255, s2, 29
	s_lshl_b32 s30, s89, 8
	s_lshl_b32 s31, s1, 4
	s_lshl_b32 s33, s89, 4
	s_lshl_b32 s3, s1, 3
	s_lshl_b32 s28, s89, 3
	v_mov_b64_e32 v[138:139], 0x2ff
	v_add_u32_e32 v145, s29, v1
	v_add_u32_e32 v146, 0, v4
	v_add_u32_e32 v147, s24, v1
	s_movk_i32 s25, 0x3000
	s_movk_i32 s77, 0x80
	s_mov_b32 s52, 0x3c800000
	s_add_i32 s53, 0, 0x20400
	s_movk_i32 s4, 0x7f
	s_mov_b32 s1, 0
	s_barrier
	s_branch .LBB0_171
